# GQA attention K tile LDS swizzle widened from 3 to 4 row bits (removes 2-way ds_read_b128 bank conflicts), on top of the expert conversion rewrite
# speedup vs baseline: 1.0037x; 1.0037x over previous
.LBB0_912:
	s_load_dwordx2 s[26:27], s[2:3], 0x78
	s_ashr_i32 s2, s54, 4
	s_mul_hi_i32 s3, s2, 0x2aaaaaab
	s_lshr_b32 s4, s3, 31
	s_add_i32 s3, s3, s4
	s_mul_i32 s3, s3, 6
	s_sub_i32 s2, s2, s3
	s_mul_hi_i32 s3, s54, 0x2aaaaaab
	s_lshr_b32 s4, s3, 31
	s_ashr_i32 s3, s3, 4
	s_add_i32 s28, s3, s4
	s_mul_i32 s3, s2, 0x56
	s_lshr_b32 s4, s3, 8
	s_bfe_u32 s3, s3, 0x1000f
	s_add_i32 s4, s4, s3
	s_ashr_i32 s29, s28, 31
	s_lshl_b32 s3, s54, 8
	s_lshl_b64 s[30:31], s[28:29], 12
	s_and_b32 s3, s3, 0xf00
	s_or_b32 s30, s30, s3
	s_sext_i32_i8 s34, s4
	s_mul_i32 s3, s31, 0x600
	s_mul_hi_u32 s4, s30, 0x600
	s_add_i32 s4, s4, s3
	s_mul_i32 s3, s30, 0x600
	s_add_u32 s5, s24, s3
	s_addc_u32 s4, s25, s4
	s_lshl_b32 s22, s2, 7
	s_ashr_i32 s23, s22, 31
	s_lshl_b64 s[2:3], s[22:23], 1
	s_add_u32 s2, s5, s2
	s_addc_u32 s3, s4, s3
	s_add_u32 s38, s2, 0x48560200
	s_addc_u32 s39, s3, 0
	s_lshl_b64 s[4:5], s[28:29], 21
	s_add_u32 s37, s24, s4
	s_addc_u32 s40, s25, s5
	s_lshl_b32 s2, s34, 7
	s_ashr_i32 s3, s2, 31
	s_lshl_b64 s[34:35], s[2:3], 1
	s_add_u32 s2, s37, s34
	s_addc_u32 s3, s40, s35
	s_add_u32 s2, s2, 0x49d60200
	s_addc_u32 s3, s3, 0
	s_lshl_b64 s[28:29], s[28:29], 25
	s_add_u32 s37, s24, s28
	s_addc_u32 s40, s25, s29
	s_add_u32 s37, s37, s34
	s_waitcnt lgkmcnt(0)
	s_addc_u32 s40, s40, s35
	s_add_u32 s52, s37, 0x40560a00
	v_ashrrev_i32_e32 v54, 4, v0
	v_lshlrev_b32_e32 v1, 3, v0
	v_ashrrev_i32_e32 v55, 31, v54
	s_addc_u32 s53, s40, 0
	v_and_b32_e32 v2, 0x78, v1
	v_lshlrev_b64 v[48:49], 13, v[54:55]
	v_lshlrev_b32_e32 v52, 1, v2
	v_add_u32_e32 v18, 32, v54
	v_lshl_add_u64 v[2:3], s[52:53], 0, v[48:49]
	v_mov_b32_e32 v53, v177
	v_lshl_add_u64 v[2:3], v[2:3], 0, v[52:53]
	v_ashrrev_i32_e32 v19, 31, v18
	global_load_dwordx4 v[2:5], v[2:3], off
	v_lshlrev_b64 v[6:7], 13, v[18:19]
	v_lshlrev_b64 v[50:51], 9, v[54:55]
	v_lshl_add_u64 v[6:7], s[52:53], 0, v[6:7]
	v_lshl_add_u64 v[10:11], s[2:3], 0, v[50:51]
	v_lshl_add_u64 v[6:7], v[6:7], 0, v[52:53]
	v_lshl_add_u64 v[10:11], v[10:11], 0, v[52:53]
	global_load_dwordx4 v[6:9], v[6:7], off
	v_lshlrev_b64 v[14:15], 9, v[18:19]
	global_load_dwordx4 v[10:13], v[10:11], off
	v_lshl_add_u64 v[14:15], s[2:3], 0, v[14:15]
	v_lshl_add_u64 v[14:15], v[14:15], 0, v[52:53]
	v_readfirstlane_b32 s37, v0
	global_load_dwordx4 v[14:17], v[14:15], off
	s_ashr_i32 s40, s37, 1
	v_mov_b32_e32 v19, s40
	v_bfe_u32 v22, v0, 5, 1
	v_bfi_b32 v19, s1, v19, v0
	v_mov_b64_e32 v[20:21], s[38:39]
	v_mad_i64_i32 v[20:21], s[38:39], v19, s0, v[20:21]
	v_lshlrev_b32_e32 v176, 4, v22
	v_lshl_add_u64 v[20:21], v[20:21], 0, v[176:177]
	global_load_dwordx4 v[124:127], v[20:21], off
	global_load_dwordx4 v[120:123], v[20:21], off offset:32
	global_load_dwordx4 v[116:119], v[20:21], off offset:64
	global_load_dwordx4 v[112:115], v[20:21], off offset:96
	global_load_dwordx4 v[108:111], v[20:21], off offset:128
	global_load_dwordx4 v[104:107], v[20:21], off offset:160
	global_load_dwordx4 v[100:103], v[20:21], off offset:192
	global_load_dwordx4 v[96:99], v[20:21], off offset:224
	v_and_b32_e32 v19, 0xfffff0, v54
	v_lshlrev_b32_e32 v20, 1, v54
	v_mov_b32_e32 v216, v22
	v_and_or_b32 v19, v20, 8, v19
	v_and_b32_e32 v22, 0xfffff0, v18
	v_lshlrev_b32_e32 v23, 1, v18
	v_lshrrev_b32_e32 v20, 1, v54
	v_lshrrev_b32_e32 v19, 1, v19
	v_bfe_u32 v1, v1, 5, 2
	v_and_b32_e32 v21, 3, v54
	v_and_or_b32 v22, v23, 8, v22
	v_or_b32_e32 v19, v19, v1
	v_and_or_b32 v20, v20, 4, v21
	v_lshrrev_b32_e32 v22, 1, v22
	v_lshlrev_b32_e32 v19, 9, v19
	v_lshlrev_b32_e32 v20, 6, v20
	v_and_b32_e32 v21, 48, v52
	v_or_b32_e32 v1, v22, v1
	v_or3_b32 v19, v19, v20, v21
	v_lshlrev_b32_e32 v1, 9, v1
	v_or3_b32 v1, v1, v20, v21
	v_add_u32_e32 v193, 0, v19
	s_waitcnt vmcnt(0)
	v_add_u32_e32 v194, 0, v1
	v_lshlrev_b32_e32 v1, 8, v54
	v_and_b32_e32 v178, 31, v0
	v_lshlrev_b32_e32 v78, 4, v0
	v_and_b32_e32 v79, 63, v0
	v_add_u32_e32 v64, 64, v54
	v_add_u32_e32 v66, 0x60, v54
	v_ashrrev_i32_e32 v65, 31, v64
	v_ashrrev_i32_e32 v67, 31, v66
	v_add_u32_e32 v72, 0xa0, v54
	v_ashrrev_i32_e32 v73, 31, v72
	v_add_u32_e32 v54, 0x80, v54
	v_lshlrev_b64 v[74:75], 9, v[72:73]
	v_lshlrev_b64 v[72:73], 13, v[72:73]
	v_lshl_add_u64 v[74:75], s[2:3], 0, v[74:75]
	v_lshl_add_u64 v[72:73], s[52:53], 0, v[72:73]
	v_lshl_add_u64 v[74:75], v[74:75], 0, v[52:53]
	v_lshl_add_u64 v[72:73], v[72:73], 0, v[52:53]
	s_and_b32 s37, s37, 0x3fffffc0
	s_lshl_b32 s37, s37, 2
	s_add_i32 s56, s37, 0
	s_add_i32 s56, s56, 0x10000
	s_and_b32 s55, s40, 0xffffffe0
	s_cmp_lg_u32 0, -1
	s_cselect_b32 s58, 0, 0
	s_mov_b32 s37, s36
	s_mov_b32 s38, s36
	s_mov_b32 s39, s36
	s_mov_b32 s40, s36
	s_mov_b32 s41, s36
	s_mov_b32 s42, s36
	s_mov_b32 s43, s36
	s_waitcnt vmcnt(11)
	ds_write_b128 v193, v[2:5]
	v_and_b32_e32 v2, 0xf0, v0
	v_bitop3_b32 v1, v52, v1, v2 bitop3:0xde
	v_add_u32_e32 v195, 0, v1
	v_lshlrev_b32_e32 v1, 8, v18
	v_bitop3_b32 v1, v52, v1, v2 bitop3:0xde
	v_add_u32_e32 v196, 0, v1
	s_waitcnt vmcnt(10)
	ds_write_b128 v194, v[6:9]
	s_mov_b32 s44, s36
	s_waitcnt vmcnt(9)
	ds_write_b128 v195, v[10:13] offset:32768
	v_lshlrev_b32_e32 v10, 8, v178
	v_and_b32_e32 v11, 0xf0, v78
	v_bitop3_b32 v1, v176, v10, v11 bitop3:0xde
	v_add_u32_e32 v197, 0, v1
	s_waitcnt vmcnt(8)
	ds_write_b128 v196, v[14:17] offset:32768
	s_waitcnt lgkmcnt(0)
	s_barrier
	ds_read_b128 v[2:5], v197 offset:32768
	ds_read_b128 v[6:9], v197 offset:40960
	s_waitcnt vmcnt(7) lgkmcnt(1)
	v_mfma_f32_32x32x16_bf16 v[32:47], v[2:5], v[124:127], 0
	v_or_b32_e32 v1, 32, v176
	v_bitop3_b32 v1, v1, v10, v11 bitop3:0xde
	v_add_u32_e32 v198, 0, v1
	v_or_b32_e32 v1, 64, v176
	v_bitop3_b32 v1, v1, v10, v11 bitop3:0xde
	v_add_u32_e32 v199, 0, v1
	v_or_b32_e32 v1, 0x60, v176
	s_waitcnt lgkmcnt(0)
	v_mfma_f32_32x32x16_bf16 v[16:31], v[6:9], v[124:127], 0
	ds_read_b128 v[2:5], v198 offset:32768
	ds_read_b128 v[6:9], v198 offset:40960
	v_bitop3_b32 v1, v1, v10, v11 bitop3:0xde
	v_add_u32_e32 v200, 0, v1
	v_or_b32_e32 v1, 0x80, v176
	v_bitop3_b32 v1, v1, v10, v11 bitop3:0xde
	v_add_u32_e32 v201, 0, v1
	v_or_b32_e32 v1, 0xa0, v176
	s_waitcnt vmcnt(6) lgkmcnt(1)
	v_mfma_f32_32x32x16_bf16 v[32:47], v[2:5], v[120:123], v[32:47]
	v_bitop3_b32 v1, v1, v10, v11 bitop3:0xde
	v_add_u32_e32 v202, 0, v1
	v_lshlrev_b32_e32 v12, 3, v79
	v_and_b32_e32 v1, 0xc0, v78
	s_mov_b32 s45, s36
	s_mov_b32 s46, s36
	s_mov_b32 s47, s36
	s_waitcnt lgkmcnt(0)
	v_mfma_f32_32x32x16_bf16 v[16:31], v[6:9], v[120:123], v[16:31]
	ds_read_b128 v[2:5], v199 offset:32768
	ds_read_b128 v[6:9], v199 offset:40960
	s_mov_b32 s48, s36
	s_mov_b32 s49, s36
	s_mov_b32 s50, s36
	s_mov_b32 s51, s36
	s_mov_b32 s57, 1
	v_lshl_add_u32 v179, v178, 2, s56
	s_waitcnt vmcnt(5) lgkmcnt(1)
	v_mfma_f32_32x32x16_bf16 v[32:47], v[2:5], v[116:119], v[32:47]
	v_mov_b32_e32 v190, 0
	s_waitcnt lgkmcnt(0)
	v_mfma_f32_32x32x16_bf16 v[16:31], v[6:9], v[116:119], v[16:31]
	ds_read_b128 v[2:5], v200 offset:32768
	ds_read_b128 v[6:9], v200 offset:40960
	s_waitcnt vmcnt(4) lgkmcnt(1)
	v_mfma_f32_32x32x16_bf16 v[32:47], v[2:5], v[112:115], v[32:47]
	s_waitcnt lgkmcnt(0)
	v_mfma_f32_32x32x16_bf16 v[16:31], v[6:9], v[112:115], v[16:31]
	ds_read_b128 v[2:5], v201 offset:32768
	ds_read_b128 v[6:9], v201 offset:40960
	s_waitcnt vmcnt(3) lgkmcnt(1)
	v_mfma_f32_32x32x16_bf16 v[32:47], v[2:5], v[108:111], v[32:47]
	ds_read_b128 v[2:5], v202 offset:32768
	s_waitcnt lgkmcnt(1)
	v_mfma_f32_32x32x16_bf16 v[16:31], v[6:9], v[108:111], v[16:31]
	ds_read_b128 v[6:9], v202 offset:40960
	s_waitcnt vmcnt(2) lgkmcnt(1)
	v_mfma_f32_32x32x16_bf16 v[32:47], v[2:5], v[104:107], v[32:47]
	v_lshlrev_b32_e32 v5, 1, v0
	v_or_b32_e32 v0, 0xc0, v176
	v_bitop3_b32 v0, v0, v10, v11 bitop3:0xde
	v_add_u32_e32 v203, 0, v0
	v_and_or_b32 v4, v12, 24, v1
	ds_read_b128 v[0:3], v203 offset:32768
	v_and_b32_e32 v5, 32, v5
	s_waitcnt lgkmcnt(1)
	v_mfma_f32_32x32x16_bf16 v[16:31], v[6:9], v[104:107], v[16:31]
	v_and_b32_e32 v6, 0x100, v12
	v_or3_b32 v80, v4, v5, v6
	ds_read_b128 v[4:7], v203 offset:40960
	v_add_u32_e32 v192, s58, v80
	s_waitcnt vmcnt(1) lgkmcnt(1)
	v_mfma_f32_32x32x16_bf16 v[32:47], v[0:3], v[100:103], v[32:47]
	v_or_b32_e32 v0, 0xe0, v176
	v_bitop3_b32 v0, v0, v10, v11 bitop3:0xde
	v_add_u32_e32 v204, 0, v0
	ds_read_b128 v[0:3], v204 offset:32768
	ds_read_b128 v[56:59], v204 offset:40960
	s_waitcnt lgkmcnt(2)
	v_mfma_f32_32x32x16_bf16 v[16:31], v[4:7], v[100:103], v[16:31]
	s_waitcnt vmcnt(0) lgkmcnt(1)
	v_mfma_f32_32x32x16_bf16 v[32:47], v[0:3], v[96:99], v[32:47]
	v_mov_b64_e32 v[0:1], s[36:37]
	v_mov_b64_e32 v[14:15], s[50:51]
	v_mov_b64_e32 v[2:3], s[38:39]
	v_mov_b64_e32 v[4:5], s[40:41]
	v_mov_b64_e32 v[6:7], s[42:43]
	v_mov_b64_e32 v[8:9], s[44:45]
	v_mov_b64_e32 v[10:11], s[46:47]
	s_waitcnt lgkmcnt(0)
	v_mfma_f32_32x32x16_bf16 v[16:31], v[56:59], v[96:99], v[16:31]
	s_nop 2
	v_max_f32_e32 v55, v33, v33
	v_max_f32_e32 v56, v32, v32
	v_max_f32_e32 v55, v56, v55
	v_max3_f32 v55, v55, v34, v35
	v_max3_f32 v55, v55, v36, v37
	v_max3_f32 v55, v55, v38, v39
	v_max3_f32 v55, v55, v40, v41
	v_max3_f32 v55, v55, v42, v43
	v_max3_f32 v55, v55, v44, v45
	v_max3_f32 v55, v55, v46, v47
	v_max3_f32 v55, v55, v16, v17
	v_max3_f32 v55, v55, v18, v19
	v_max3_f32 v55, v55, v20, v21
	v_max3_f32 v55, v55, v22, v23
	v_max3_f32 v55, v55, v24, v25
	v_max3_f32 v55, v55, v26, v27
	v_lshlrev_b64 v[56:57], 13, v[64:65]
	v_lshlrev_b64 v[58:59], 13, v[66:67]
	v_lshlrev_b64 v[64:65], 9, v[64:65]
	v_lshlrev_b64 v[66:67], 9, v[66:67]
	v_max3_f32 v55, v55, v28, v29
	v_lshl_add_u64 v[56:57], s[52:53], 0, v[56:57]
	v_lshl_add_u64 v[58:59], s[52:53], 0, v[58:59]
	v_lshl_add_u64 v[64:65], s[2:3], 0, v[64:65]
	v_lshl_add_u64 v[66:67], s[2:3], 0, v[66:67]
	v_max3_f32 v81, v55, v30, v31
	v_lshl_add_u64 v[56:57], v[56:57], 0, v[52:53]
	v_lshl_add_u64 v[60:61], v[58:59], 0, v[52:53]
	v_lshl_add_u64 v[64:65], v[64:65], 0, v[52:53]
	v_lshl_add_u64 v[68:69], v[66:67], 0, v[52:53]
	v_ashrrev_i32_e32 v55, 31, v54
	global_load_dwordx4 v[56:59], v[56:57], off
	s_nop 0
	global_load_dwordx4 v[60:63], v[60:61], off
	s_nop 0
	global_load_dwordx4 v[64:67], v[64:65], off
	s_nop 0
	global_load_dwordx4 v[68:71], v[68:69], off
	v_lshlrev_b64 v[76:77], 9, v[54:55]
	v_lshlrev_b64 v[54:55], 13, v[54:55]
	v_lshl_add_u64 v[76:77], s[2:3], 0, v[76:77]
	v_lshl_add_u64 v[54:55], s[52:53], 0, v[54:55]
	v_lshl_add_u64 v[76:77], v[76:77], 0, v[52:53]
	global_load_dwordx4 v[140:143], v[74:75], off
	global_load_dwordx4 v[136:139], v[76:77], off
	v_lshl_add_u64 v[52:53], v[54:55], 0, v[52:53]
	global_load_dwordx4 v[132:135], v[72:73], off
	global_load_dwordx4 v[128:131], v[52:53], off
	v_mov_b32_e32 v82, v81
	s_nop 1
	v_permlane32_swap_b32_e32 v81, v82
	v_max_f32_e32 v52, v82, v82
	v_max_f32_e32 v53, v81, v81
	v_max_f32_e32 v52, v53, v52
	v_add_f32_e32 v53, 0x7149f2ca, v52
	v_max_f32_e32 v52, 0xf149f2ca, v52
	v_cmp_ge_f32_e32 vcc, s9, v53
	v_sub_f32_e32 v53, 0xf149f2ca, v52
	v_mul_f32_e32 v53, 0x3e0293ee, v53
	v_exp_f32_e32 v53, v53
	s_cmp_eq_u64 vcc, exec
	s_cselect_b64 vcc, -1, 0
	v_mov_b32_e32 v54, 0xf149f2ca
	v_cndmask_b32_e32 v160, v52, v54, vcc
	v_mul_f32_e32 v52, 0xbe0293ee, v160
	v_cndmask_b32_e64 v205, v53, 1.0, vcc
	v_mov_b32_e32 v53, v52
	v_fmac_f32_e32 v53, 0x3e0293ee, v47
	v_pk_fma_f32 v[150:151], v[18:19], s[8:9], v[52:53] op_sel_hi:[1,0,0]
	v_pk_fma_f32 v[152:153], v[16:17], s[8:9], v[52:53] op_sel_hi:[1,0,0]
	v_lshl_add_u64 v[16:17], s[4:5], 0, v[50:51]
	v_and_b32_e32 v18, 0xf0, v78
	v_fmamk_f32 v32, v32, 0x3e0293ee, v52
	v_fmamk_f32 v33, v33, 0x3e0293ee, v52
	v_fmamk_f32 v34, v34, 0x3e0293ee, v52
	v_fmamk_f32 v35, v35, 0x3e0293ee, v52
	v_fmamk_f32 v36, v36, 0x3e0293ee, v52
	v_fmamk_f32 v37, v37, 0x3e0293ee, v52
	v_fmamk_f32 v38, v38, 0x3e0293ee, v52
	v_fmamk_f32 v39, v39, 0x3e0293ee, v52
	v_fmamk_f32 v40, v40, 0x3e0293ee, v52
	v_fmamk_f32 v41, v41, 0x3e0293ee, v52
	v_fmamk_f32 v42, v42, 0x3e0293ee, v52
	v_fmamk_f32 v43, v43, 0x3e0293ee, v52
	v_fmamk_f32 v44, v44, 0x3e0293ee, v52
	v_fmamk_f32 v45, v45, 0x3e0293ee, v52
	v_fmamk_f32 v46, v46, 0x3e0293ee, v52
	v_or_b32_e32 v16, v16, v18
	v_exp_f32_e32 v170, v32
	v_exp_f32_e32 v171, v33
	v_exp_f32_e32 v172, v34
	v_exp_f32_e32 v173, v35
	v_exp_f32_e32 v174, v36
	v_exp_f32_e32 v184, v37
	v_exp_f32_e32 v175, v38
	v_exp_f32_e32 v185, v39
	v_exp_f32_e32 v162, v40
	v_exp_f32_e32 v163, v41
	v_exp_f32_e32 v164, v42
	v_exp_f32_e32 v166, v43
	v_exp_f32_e32 v165, v44
	v_exp_f32_e32 v167, v45
	v_exp_f32_e32 v168, v46
	v_exp_f32_e32 v169, v53
	v_lshl_add_u64 v[180:181], s[24:25], 0, v[16:17]
	v_lshl_add_u64 v[16:17], s[28:29], 0, v[48:49]
	s_waitcnt vmcnt(4)
	v_or_b32_e32 v16, v16, v18
	v_mov_b64_e32 v[12:13], s[48:49]
	v_pk_fma_f32 v[154:155], v[30:31], s[8:9], v[52:53] op_sel_hi:[1,0,0]
	v_pk_fma_f32 v[156:157], v[28:29], s[8:9], v[52:53] op_sel_hi:[1,0,0]
	v_pk_fma_f32 v[158:159], v[26:27], s[8:9], v[52:53] op_sel_hi:[1,0,0]
	v_pk_fma_f32 v[144:145], v[24:25], s[8:9], v[52:53] op_sel_hi:[1,0,0]
	v_pk_fma_f32 v[146:147], v[22:23], s[8:9], v[52:53] op_sel_hi:[1,0,0]
	v_pk_fma_f32 v[148:149], v[20:21], s[8:9], v[52:53] op_sel_hi:[1,0,0]
	s_waitcnt vmcnt(7)
	ds_write_b128 v193, v[56:59] offset:16384
	s_waitcnt vmcnt(6)
	ds_write_b128 v194, v[60:63] offset:16384
	s_waitcnt vmcnt(5)
	ds_write_b128 v195, v[64:67] offset:49152
	s_waitcnt vmcnt(4)
	ds_write_b128 v196, v[68:71] offset:49152
	s_addk_i32 s58, 0x4000
	v_lshl_add_u64 v[182:183], s[24:25], 0, v[16:17]
	v_mov_b64_e32 v[62:63], v[14:15]
	v_mov_b64_e32 v[30:31], v[14:15]
	v_mov_b64_e32 v[46:47], v[14:15]
	v_cmp_gt_u32_e64 s[2:3], 32, v79
	v_add_u32_e32 v191, s58, v80
	v_mov_b64_e32 v[60:61], v[12:13]
	v_mov_b64_e32 v[58:59], v[10:11]
	v_mov_b64_e32 v[56:57], v[8:9]
	v_mov_b64_e32 v[54:55], v[6:7]
	v_mov_b64_e32 v[52:53], v[4:5]
	v_mov_b64_e32 v[50:51], v[2:3]
	v_mov_b64_e32 v[48:49], v[0:1]
	v_mov_b64_e32 v[28:29], v[12:13]
	v_mov_b64_e32 v[26:27], v[10:11]
	v_mov_b64_e32 v[24:25], v[8:9]
	v_mov_b64_e32 v[22:23], v[6:7]
	v_mov_b64_e32 v[20:21], v[4:5]
	v_mov_b64_e32 v[18:19], v[2:3]
	v_mov_b64_e32 v[16:17], v[0:1]
	v_mov_b64_e32 v[44:45], v[12:13]
	v_mov_b64_e32 v[42:43], v[10:11]
	v_mov_b64_e32 v[40:41], v[8:9]
	v_mov_b64_e32 v[38:39], v[6:7]
	v_mov_b64_e32 v[36:37], v[4:5]
	v_mov_b64_e32 v[34:35], v[2:3]
	v_mov_b64_e32 v[32:33], v[0:1]
	s_waitcnt lgkmcnt(0)
	s_barrier

.LBB0_2189:
	s_load_dwordx2 s[30:31], s[2:3], 0x78
	s_ashr_i32 s2, s57, 4
	s_mul_hi_i32 s3, s2, 0x2aaaaaab
	s_lshr_b32 s4, s3, 31
	s_add_i32 s3, s3, s4
	s_mul_i32 s3, s3, 6
	s_sub_i32 s2, s2, s3
	s_mul_hi_i32 s3, s57, 0x2aaaaaab
	s_lshr_b32 s4, s3, 31
	s_ashr_i32 s3, s3, 4
	s_add_i32 s28, s3, s4
	s_mul_i32 s3, s2, 0x56
	s_lshr_b32 s4, s3, 8
	s_bfe_u32 s3, s3, 0x1000f
	s_add_i32 s4, s4, s3
	s_ashr_i32 s29, s28, 31
	s_lshl_b32 s3, s57, 8
	s_lshl_b64 s[34:35], s[28:29], 12
	s_and_b32 s3, s3, 0xf00
	s_or_b32 s34, s34, s3
	s_sext_i32_i8 s37, s4
	s_mul_i32 s3, s35, 0x600
	s_mul_hi_u32 s4, s34, 0x600
	s_add_i32 s4, s4, s3
	s_mul_i32 s3, s34, 0x600
	s_add_u32 s5, s26, s3
	s_addc_u32 s4, s27, s4
	s_lshl_b32 s24, s2, 7
	s_ashr_i32 s25, s24, 31
	s_lshl_b64 s[2:3], s[24:25], 1
	s_add_u32 s2, s5, s2
	s_addc_u32 s3, s4, s3
	s_add_u32 s38, s2, 0x48560200
	s_addc_u32 s39, s3, 0
	s_lshl_b64 s[4:5], s[28:29], 21
	s_add_u32 s40, s26, s4
	s_addc_u32 s41, s27, s5
	s_lshl_b32 s2, s37, 7
	s_ashr_i32 s3, s2, 31
	s_lshl_b64 s[52:53], s[2:3], 1
	s_add_u32 s2, s40, s52
	s_addc_u32 s3, s41, s53
	s_add_u32 s2, s2, 0x49d60200
	s_addc_u32 s3, s3, 0
	s_lshl_b64 s[28:29], s[28:29], 25
	s_add_u32 s37, s26, s28
	s_addc_u32 s40, s27, s29
	s_add_u32 s37, s37, s52
	s_waitcnt lgkmcnt(0)
	s_addc_u32 s40, s40, s53
	s_add_u32 s54, s37, 0x40560a00
	v_ashrrev_i32_e32 v54, 4, v0
	v_lshlrev_b32_e32 v1, 3, v0
	v_ashrrev_i32_e32 v55, 31, v54
	s_addc_u32 s55, s40, 0
	v_and_b32_e32 v2, 0x78, v1
	v_lshlrev_b64 v[48:49], 13, v[54:55]
	v_lshlrev_b32_e32 v52, 1, v2
	v_add_u32_e32 v18, 32, v54
	v_lshl_add_u64 v[2:3], s[54:55], 0, v[48:49]
	v_mov_b32_e32 v53, v177
	v_lshl_add_u64 v[2:3], v[2:3], 0, v[52:53]
	v_ashrrev_i32_e32 v19, 31, v18
	global_load_dwordx4 v[2:5], v[2:3], off
	v_lshlrev_b64 v[6:7], 13, v[18:19]
	v_lshlrev_b64 v[50:51], 9, v[54:55]
	v_lshl_add_u64 v[6:7], s[54:55], 0, v[6:7]
	v_lshl_add_u64 v[10:11], s[2:3], 0, v[50:51]
	v_lshl_add_u64 v[6:7], v[6:7], 0, v[52:53]
	v_lshl_add_u64 v[10:11], v[10:11], 0, v[52:53]
	global_load_dwordx4 v[6:9], v[6:7], off
	v_lshlrev_b64 v[14:15], 9, v[18:19]
	global_load_dwordx4 v[10:13], v[10:11], off
	v_lshl_add_u64 v[14:15], s[2:3], 0, v[14:15]
	v_lshl_add_u64 v[14:15], v[14:15], 0, v[52:53]
	v_readfirstlane_b32 s37, v0
	global_load_dwordx4 v[14:17], v[14:15], off
	s_ashr_i32 s40, s37, 1
	v_mov_b32_e32 v19, s40
	v_bfe_u32 v189, v0, 5, 1
	v_bfi_b32 v19, s1, v19, v0
	v_mov_b64_e32 v[20:21], s[38:39]
	v_mad_i64_i32 v[20:21], s[38:39], v19, s0, v[20:21]
	v_lshlrev_b32_e32 v176, 4, v189
	v_lshl_add_u64 v[20:21], v[20:21], 0, v[176:177]
	global_load_dwordx4 v[124:127], v[20:21], off
	global_load_dwordx4 v[120:123], v[20:21], off offset:32
	global_load_dwordx4 v[116:119], v[20:21], off offset:64
	global_load_dwordx4 v[112:115], v[20:21], off offset:96
	global_load_dwordx4 v[108:111], v[20:21], off offset:128
	global_load_dwordx4 v[104:107], v[20:21], off offset:160
	global_load_dwordx4 v[100:103], v[20:21], off offset:192
	global_load_dwordx4 v[96:99], v[20:21], off offset:224
	v_and_b32_e32 v19, 0xfffff0, v54
	v_lshlrev_b32_e32 v20, 1, v54
	v_and_or_b32 v19, v20, 8, v19
	v_and_b32_e32 v22, 0xfffff0, v18
	v_lshlrev_b32_e32 v23, 1, v18
	v_lshrrev_b32_e32 v20, 1, v54
	v_lshrrev_b32_e32 v19, 1, v19
	v_bfe_u32 v1, v1, 5, 2
	v_and_b32_e32 v21, 3, v54
	v_and_or_b32 v22, v23, 8, v22
	v_or_b32_e32 v19, v19, v1
	v_and_or_b32 v20, v20, 4, v21
	v_lshrrev_b32_e32 v22, 1, v22
	v_lshlrev_b32_e32 v19, 9, v19
	v_lshlrev_b32_e32 v20, 6, v20
	v_and_b32_e32 v21, 48, v52
	v_or_b32_e32 v1, v22, v1
	v_or3_b32 v19, v19, v20, v21
	v_lshlrev_b32_e32 v1, 9, v1
	v_or3_b32 v1, v1, v20, v21
	v_add_u32_e32 v193, 0, v19
	s_waitcnt vmcnt(0)
	v_add_u32_e32 v194, 0, v1
	v_lshlrev_b32_e32 v1, 8, v54
	v_and_b32_e32 v178, 31, v0
	v_lshlrev_b32_e32 v78, 4, v0
	v_and_b32_e32 v79, 63, v0
	v_add_u32_e32 v64, 64, v54
	v_add_u32_e32 v66, 0x60, v54
	v_ashrrev_i32_e32 v65, 31, v64
	v_ashrrev_i32_e32 v67, 31, v66
	v_add_u32_e32 v72, 0xa0, v54
	v_ashrrev_i32_e32 v73, 31, v72
	v_add_u32_e32 v54, 0x80, v54
	v_lshlrev_b64 v[74:75], 9, v[72:73]
	v_lshlrev_b64 v[72:73], 13, v[72:73]
	v_lshl_add_u64 v[74:75], s[2:3], 0, v[74:75]
	v_lshl_add_u64 v[72:73], s[54:55], 0, v[72:73]
	v_lshl_add_u64 v[74:75], v[74:75], 0, v[52:53]
	v_lshl_add_u64 v[72:73], v[72:73], 0, v[52:53]
	s_and_b32 s37, s37, 0x3fffffc0
	s_lshl_b32 s37, s37, 2
	s_add_i32 s59, s37, 0
	s_add_i32 s59, s59, 0x10000
	s_and_b32 s58, s40, 0xffffffe0
	s_cmp_lg_u32 0, -1
	s_cselect_b32 s61, 0, 0
	s_mov_b32 s37, s36
	s_mov_b32 s38, s36
	s_mov_b32 s39, s36
	s_mov_b32 s40, s36
	s_mov_b32 s41, s36
	s_mov_b32 s42, s36
	s_mov_b32 s43, s36
	s_mov_b32 s44, s36
	s_waitcnt vmcnt(11)
	ds_write_b128 v193, v[2:5]
	v_and_b32_e32 v2, 0xf0, v0
	v_bitop3_b32 v1, v52, v1, v2 bitop3:0xde
	v_add_u32_e32 v195, 0, v1
	v_lshlrev_b32_e32 v1, 8, v18
	v_bitop3_b32 v1, v52, v1, v2 bitop3:0xde
	v_add_u32_e32 v196, 0, v1
	s_waitcnt vmcnt(10)
	ds_write_b128 v194, v[6:9]
	s_mov_b32 s45, s36
	s_waitcnt vmcnt(9)
	ds_write_b128 v195, v[10:13] offset:32768
	v_lshlrev_b32_e32 v10, 8, v178
	v_and_b32_e32 v11, 0xf0, v78
	v_bitop3_b32 v1, v176, v10, v11 bitop3:0xde
	v_add_u32_e32 v197, 0, v1
	s_waitcnt vmcnt(8)
	ds_write_b128 v196, v[14:17] offset:32768
	s_waitcnt lgkmcnt(0)
	s_barrier
	ds_read_b128 v[2:5], v197 offset:32768
	ds_read_b128 v[6:9], v197 offset:40960
	s_waitcnt vmcnt(7) lgkmcnt(1)
	v_mfma_f32_32x32x16_bf16 v[32:47], v[2:5], v[124:127], 0
	v_or_b32_e32 v1, 32, v176
	v_bitop3_b32 v1, v1, v10, v11 bitop3:0xde
	v_add_u32_e32 v198, 0, v1
	v_or_b32_e32 v1, 64, v176
	v_bitop3_b32 v1, v1, v10, v11 bitop3:0xde
	v_add_u32_e32 v199, 0, v1
	v_or_b32_e32 v1, 0x60, v176
	s_waitcnt lgkmcnt(0)
	v_mfma_f32_32x32x16_bf16 v[16:31], v[6:9], v[124:127], 0
	ds_read_b128 v[2:5], v198 offset:32768
	ds_read_b128 v[6:9], v198 offset:40960
	v_bitop3_b32 v1, v1, v10, v11 bitop3:0xde
	v_add_u32_e32 v200, 0, v1
	v_or_b32_e32 v1, 0x80, v176
	v_bitop3_b32 v1, v1, v10, v11 bitop3:0xde
	v_add_u32_e32 v201, 0, v1
	v_or_b32_e32 v1, 0xa0, v176
	s_waitcnt vmcnt(6) lgkmcnt(1)
	v_mfma_f32_32x32x16_bf16 v[32:47], v[2:5], v[120:123], v[32:47]
	v_bitop3_b32 v1, v1, v10, v11 bitop3:0xde
	v_add_u32_e32 v202, 0, v1
	v_lshlrev_b32_e32 v12, 3, v79
	v_and_b32_e32 v1, 0xc0, v78
	s_mov_b32 s46, s36
	s_mov_b32 s47, s36
	s_mov_b32 s48, s36
	s_waitcnt lgkmcnt(0)
	v_mfma_f32_32x32x16_bf16 v[16:31], v[6:9], v[120:123], v[16:31]
	ds_read_b128 v[2:5], v199 offset:32768
	ds_read_b128 v[6:9], v199 offset:40960
	s_mov_b32 s49, s36
	s_mov_b32 s50, s36
	s_mov_b32 s51, s36
	s_mov_b32 s60, 1
	v_lshl_add_u32 v179, v178, 2, s59
	v_mov_b32_e32 v190, 0
	s_waitcnt vmcnt(5) lgkmcnt(1)
	v_mfma_f32_32x32x16_bf16 v[32:47], v[2:5], v[116:119], v[32:47]
	s_waitcnt lgkmcnt(0)
	v_mfma_f32_32x32x16_bf16 v[16:31], v[6:9], v[116:119], v[16:31]
	ds_read_b128 v[2:5], v200 offset:32768
	ds_read_b128 v[6:9], v200 offset:40960
	s_waitcnt vmcnt(4) lgkmcnt(1)
	v_mfma_f32_32x32x16_bf16 v[32:47], v[2:5], v[112:115], v[32:47]
	s_waitcnt lgkmcnt(0)
	v_mfma_f32_32x32x16_bf16 v[16:31], v[6:9], v[112:115], v[16:31]
	ds_read_b128 v[2:5], v201 offset:32768
	ds_read_b128 v[6:9], v201 offset:40960
	s_waitcnt vmcnt(3) lgkmcnt(1)
	v_mfma_f32_32x32x16_bf16 v[32:47], v[2:5], v[108:111], v[32:47]
	ds_read_b128 v[2:5], v202 offset:32768
	s_waitcnt lgkmcnt(1)
	v_mfma_f32_32x32x16_bf16 v[16:31], v[6:9], v[108:111], v[16:31]
	ds_read_b128 v[6:9], v202 offset:40960
	s_waitcnt vmcnt(2) lgkmcnt(1)
	v_mfma_f32_32x32x16_bf16 v[32:47], v[2:5], v[104:107], v[32:47]
	v_lshlrev_b32_e32 v5, 1, v0
	v_or_b32_e32 v0, 0xc0, v176
	v_bitop3_b32 v0, v0, v10, v11 bitop3:0xde
	v_add_u32_e32 v203, 0, v0
	v_and_or_b32 v4, v12, 24, v1
	ds_read_b128 v[0:3], v203 offset:32768
	v_and_b32_e32 v5, 32, v5
	s_waitcnt lgkmcnt(1)
	v_mfma_f32_32x32x16_bf16 v[16:31], v[6:9], v[104:107], v[16:31]
	v_and_b32_e32 v6, 0x100, v12
	v_or3_b32 v80, v4, v5, v6
	ds_read_b128 v[4:7], v203 offset:40960
	v_add_u32_e32 v192, s61, v80
	s_waitcnt vmcnt(1) lgkmcnt(1)
	v_mfma_f32_32x32x16_bf16 v[32:47], v[0:3], v[100:103], v[32:47]
	v_or_b32_e32 v0, 0xe0, v176
	v_bitop3_b32 v0, v0, v10, v11 bitop3:0xde
	v_add_u32_e32 v204, 0, v0
	ds_read_b128 v[0:3], v204 offset:32768
	ds_read_b128 v[56:59], v204 offset:40960
	s_waitcnt lgkmcnt(2)
	v_mfma_f32_32x32x16_bf16 v[16:31], v[4:7], v[100:103], v[16:31]
	s_waitcnt vmcnt(0) lgkmcnt(1)
	v_mfma_f32_32x32x16_bf16 v[32:47], v[0:3], v[96:99], v[32:47]
	v_mov_b64_e32 v[0:1], s[36:37]
	v_mov_b64_e32 v[14:15], s[50:51]
	v_mov_b64_e32 v[2:3], s[38:39]
	v_mov_b64_e32 v[4:5], s[40:41]
	v_mov_b64_e32 v[6:7], s[42:43]
	v_mov_b64_e32 v[8:9], s[44:45]
	v_mov_b64_e32 v[10:11], s[46:47]
	s_waitcnt lgkmcnt(0)
	v_mfma_f32_32x32x16_bf16 v[16:31], v[56:59], v[96:99], v[16:31]
	s_nop 2
	v_max_f32_e32 v55, v33, v33
	v_max_f32_e32 v56, v32, v32
	v_max_f32_e32 v55, v56, v55
	v_max3_f32 v55, v55, v34, v35
	v_max3_f32 v55, v55, v36, v37
	v_max3_f32 v55, v55, v38, v39
	v_max3_f32 v55, v55, v40, v41
	v_max3_f32 v55, v55, v42, v43
	v_max3_f32 v55, v55, v44, v45
	v_max3_f32 v55, v55, v46, v47
	v_max3_f32 v55, v55, v16, v17
	v_max3_f32 v55, v55, v18, v19
	v_max3_f32 v55, v55, v20, v21
	v_max3_f32 v55, v55, v22, v23
	v_max3_f32 v55, v55, v24, v25
	v_max3_f32 v55, v55, v26, v27
	v_lshlrev_b64 v[56:57], 13, v[64:65]
	v_lshlrev_b64 v[58:59], 13, v[66:67]
	v_lshlrev_b64 v[64:65], 9, v[64:65]
	v_lshlrev_b64 v[66:67], 9, v[66:67]
	v_max3_f32 v55, v55, v28, v29
	v_lshl_add_u64 v[56:57], s[54:55], 0, v[56:57]
	v_lshl_add_u64 v[58:59], s[54:55], 0, v[58:59]
	v_lshl_add_u64 v[64:65], s[2:3], 0, v[64:65]
	v_lshl_add_u64 v[66:67], s[2:3], 0, v[66:67]
	v_max3_f32 v81, v55, v30, v31
	v_lshl_add_u64 v[56:57], v[56:57], 0, v[52:53]
	v_lshl_add_u64 v[60:61], v[58:59], 0, v[52:53]
	v_lshl_add_u64 v[64:65], v[64:65], 0, v[52:53]
	v_lshl_add_u64 v[68:69], v[66:67], 0, v[52:53]
	v_ashrrev_i32_e32 v55, 31, v54
	global_load_dwordx4 v[56:59], v[56:57], off
	s_nop 0
	global_load_dwordx4 v[60:63], v[60:61], off
	s_nop 0
	global_load_dwordx4 v[64:67], v[64:65], off
	s_nop 0
	global_load_dwordx4 v[68:71], v[68:69], off
	v_lshlrev_b64 v[76:77], 9, v[54:55]
	v_lshlrev_b64 v[54:55], 13, v[54:55]
	v_lshl_add_u64 v[76:77], s[2:3], 0, v[76:77]
	v_lshl_add_u64 v[54:55], s[54:55], 0, v[54:55]
	v_lshl_add_u64 v[76:77], v[76:77], 0, v[52:53]
	global_load_dwordx4 v[140:143], v[74:75], off
	global_load_dwordx4 v[136:139], v[76:77], off
	v_lshl_add_u64 v[52:53], v[54:55], 0, v[52:53]
	global_load_dwordx4 v[132:135], v[72:73], off
	global_load_dwordx4 v[128:131], v[52:53], off
	v_mov_b32_e32 v82, v81
	s_nop 1
	v_permlane32_swap_b32_e32 v81, v82
	v_max_f32_e32 v52, v82, v82
	v_max_f32_e32 v53, v81, v81
	v_max_f32_e32 v52, v53, v52
	v_add_f32_e32 v53, 0x7149f2ca, v52
	v_max_f32_e32 v52, 0xf149f2ca, v52
	v_cmp_ge_f32_e32 vcc, s9, v53
	v_sub_f32_e32 v53, 0xf149f2ca, v52
	v_mul_f32_e32 v53, 0x3e0293ee, v53
	v_exp_f32_e32 v53, v53
	s_cmp_eq_u64 vcc, exec
	s_cselect_b64 vcc, -1, 0
	v_cndmask_b32_e32 v160, v52, v188, vcc
	v_mul_f32_e32 v52, 0xbe0293ee, v160
	v_cndmask_b32_e64 v205, v53, 1.0, vcc
	v_mov_b32_e32 v53, v52
	v_fmac_f32_e32 v53, 0x3e0293ee, v47
	v_pk_fma_f32 v[150:151], v[18:19], s[8:9], v[52:53] op_sel_hi:[1,0,0]
	v_pk_fma_f32 v[152:153], v[16:17], s[8:9], v[52:53] op_sel_hi:[1,0,0]
	v_lshl_add_u64 v[16:17], s[4:5], 0, v[50:51]
	v_and_b32_e32 v18, 0xf0, v78
	v_fmamk_f32 v32, v32, 0x3e0293ee, v52
	v_fmamk_f32 v33, v33, 0x3e0293ee, v52
	v_fmamk_f32 v34, v34, 0x3e0293ee, v52
	v_fmamk_f32 v35, v35, 0x3e0293ee, v52
	v_fmamk_f32 v36, v36, 0x3e0293ee, v52
	v_fmamk_f32 v37, v37, 0x3e0293ee, v52
	v_fmamk_f32 v38, v38, 0x3e0293ee, v52
	v_fmamk_f32 v39, v39, 0x3e0293ee, v52
	v_fmamk_f32 v40, v40, 0x3e0293ee, v52
	v_fmamk_f32 v41, v41, 0x3e0293ee, v52
	v_fmamk_f32 v42, v42, 0x3e0293ee, v52
	v_fmamk_f32 v43, v43, 0x3e0293ee, v52
	v_fmamk_f32 v44, v44, 0x3e0293ee, v52
	v_fmamk_f32 v45, v45, 0x3e0293ee, v52
	v_fmamk_f32 v46, v46, 0x3e0293ee, v52
	v_or_b32_e32 v16, v16, v18
	v_exp_f32_e32 v170, v32
	v_exp_f32_e32 v171, v33
	v_exp_f32_e32 v172, v34
	v_exp_f32_e32 v173, v35
	v_exp_f32_e32 v174, v36
	v_exp_f32_e32 v184, v37
	v_exp_f32_e32 v175, v38
	v_exp_f32_e32 v185, v39
	v_exp_f32_e32 v162, v40
	v_exp_f32_e32 v163, v41
	v_exp_f32_e32 v164, v42
	v_exp_f32_e32 v166, v43
	v_exp_f32_e32 v165, v44
	v_exp_f32_e32 v167, v45
	v_exp_f32_e32 v168, v46
	v_exp_f32_e32 v169, v53
	v_lshl_add_u64 v[180:181], s[26:27], 0, v[16:17]
	v_lshl_add_u64 v[16:17], s[28:29], 0, v[48:49]
	s_waitcnt vmcnt(4)
	v_or_b32_e32 v16, v16, v18
	v_mov_b64_e32 v[12:13], s[48:49]
	v_pk_fma_f32 v[154:155], v[30:31], s[8:9], v[52:53] op_sel_hi:[1,0,0]
	v_pk_fma_f32 v[156:157], v[28:29], s[8:9], v[52:53] op_sel_hi:[1,0,0]
	v_pk_fma_f32 v[158:159], v[26:27], s[8:9], v[52:53] op_sel_hi:[1,0,0]
	v_pk_fma_f32 v[144:145], v[24:25], s[8:9], v[52:53] op_sel_hi:[1,0,0]
	v_pk_fma_f32 v[146:147], v[22:23], s[8:9], v[52:53] op_sel_hi:[1,0,0]
	v_pk_fma_f32 v[148:149], v[20:21], s[8:9], v[52:53] op_sel_hi:[1,0,0]
	s_waitcnt vmcnt(7)
	ds_write_b128 v193, v[56:59] offset:16384
	s_waitcnt vmcnt(6)
	ds_write_b128 v194, v[60:63] offset:16384
	s_waitcnt vmcnt(5)
	ds_write_b128 v195, v[64:67] offset:49152
	s_waitcnt vmcnt(4)
	ds_write_b128 v196, v[68:71] offset:49152
	s_addk_i32 s61, 0x4000
	v_lshl_add_u64 v[182:183], s[26:27], 0, v[16:17]
	v_mov_b64_e32 v[62:63], v[14:15]
	v_mov_b64_e32 v[30:31], v[14:15]
	v_mov_b64_e32 v[46:47], v[14:15]
	v_cmp_gt_u32_e64 s[2:3], 32, v79
	v_add_u32_e32 v191, s61, v80
	v_mov_b64_e32 v[60:61], v[12:13]
	v_mov_b64_e32 v[58:59], v[10:11]
	v_mov_b64_e32 v[56:57], v[8:9]
	v_mov_b64_e32 v[54:55], v[6:7]
	v_mov_b64_e32 v[52:53], v[4:5]
	v_mov_b64_e32 v[50:51], v[2:3]
	v_mov_b64_e32 v[48:49], v[0:1]
	v_mov_b64_e32 v[28:29], v[12:13]
	v_mov_b64_e32 v[26:27], v[10:11]
	v_mov_b64_e32 v[24:25], v[8:9]
	v_mov_b64_e32 v[22:23], v[6:7]
	v_mov_b64_e32 v[20:21], v[4:5]
	v_mov_b64_e32 v[18:19], v[2:3]
	v_mov_b64_e32 v[16:17], v[0:1]
	v_mov_b64_e32 v[44:45], v[12:13]
	v_mov_b64_e32 v[42:43], v[10:11]
	v_mov_b64_e32 v[40:41], v[8:9]
	v_mov_b64_e32 v[38:39], v[6:7]
	v_mov_b64_e32 v[36:37], v[4:5]
	v_mov_b64_e32 v[34:35], v[2:3]
	v_mov_b64_e32 v[32:33], v[0:1]
	s_waitcnt lgkmcnt(0)
	s_barrier
